# v035 plus next-tile V loads issued between the K-tile ds_writes (redundant vmcnt ladder behind the asm vmcnt(0) dropped)
# baseline (speedup 1.0000x reference)
; #define LAS __attribute__((address_space(3)))
; __device__ __forceinline__ void qkt(f32x16& p0, f32x16& p1, const LAS char* Ks, const bf16x8* qr, int r32, int hi) {
;   p0 = f32x16{}; p1 = f32x16{};
; #pragma unroll
;   for (int d0 = 0; d0 < 8; ++d0) { int cb = (d0 * 16 + hi * 8) * 2;
;     bf16x8 b0 = *(const LAS bf16x8*)(Ks + KSWZ(r32, cb));
;     bf16x8 b1 = *(const LAS bf16x8*)(Ks + KSWZ(32 + r32, cb));
;     p0 = __builtin_amdgcn_mfma_f32_32x32x16_bf16(b0, qr[d0], p0, 0, 0, 0);
;     p1 = __builtin_amdgcn_mfma_f32_32x32x16_bf16(b1, qr[d0], p1, 0, 0, 0); }
; }
.LBB0_936:
	s_waitcnt lgkmcnt(3)
	v_mfma_f32_32x32x16_bf16 v[148:163], v[132:135], v[164:167], 0
	s_mov_b32 s8, 0x42b504f3
	s_waitcnt lgkmcnt(2)
	v_mfma_f32_32x32x16_bf16 v[132:147], v[136:139], v[164:167], 0
	s_waitcnt lgkmcnt(1)
	v_mfma_f32_32x32x16_bf16 v[148:163], v[250:253], v[168:171], v[148:163]
	ds_read_b128 v[250:253], v246 offset:8192
	s_waitcnt lgkmcnt(1)
	v_mfma_f32_32x32x16_bf16 v[132:147], v[222:225], v[168:171], v[132:147]
	ds_read_b128 v[222:225], v246
	v_add_u32_e32 v246, v2, v235
	s_waitcnt lgkmcnt(1)
	v_mfma_f32_32x32x16_bf16 v[132:147], v[250:253], v[172:175], v[132:147]
	ds_read_b128 v[250:253], v246 offset:8192
	s_waitcnt lgkmcnt(1)
	v_mfma_f32_32x32x16_bf16 v[148:163], v[222:225], v[172:175], v[148:163]
	ds_read_b128 v[222:225], v246
	v_add_u32_e32 v246, v2, v236
	s_waitcnt lgkmcnt(1)
	v_mfma_f32_32x32x16_bf16 v[132:147], v[250:253], v[176:179], v[132:147]
	ds_read_b128 v[250:253], v246 offset:8192
	s_waitcnt lgkmcnt(1)
	v_mfma_f32_32x32x16_bf16 v[148:163], v[222:225], v[176:179], v[148:163]
	ds_read_b128 v[222:225], v246
	v_add_u32_e32 v246, v2, v237
	s_waitcnt lgkmcnt(1)
	v_mfma_f32_32x32x16_bf16 v[132:147], v[250:253], v[180:183], v[132:147]
	ds_read_b128 v[250:253], v246 offset:8192
	s_waitcnt lgkmcnt(1)
	v_mfma_f32_32x32x16_bf16 v[148:163], v[222:225], v[180:183], v[148:163]
	ds_read_b128 v[222:225], v246
	v_add_u32_e32 v246, v2, v238
	v_add_u32_e32 v2, v2, v242
	s_waitcnt lgkmcnt(1)
	v_mfma_f32_32x32x16_bf16 v[132:147], v[250:253], v[184:187], v[132:147]
	ds_read_b128 v[250:253], v246 offset:8192
	s_waitcnt lgkmcnt(1)
	v_mfma_f32_32x32x16_bf16 v[148:163], v[222:225], v[184:187], v[148:163]
	ds_read_b128 v[222:225], v246
	s_waitcnt lgkmcnt(1)
	v_mfma_f32_32x32x16_bf16 v[132:147], v[250:253], v[188:191], v[132:147]
	ds_read_b128 v[250:253], v2 offset:8192
	s_waitcnt lgkmcnt(1)
	v_mfma_f32_32x32x16_bf16 v[148:163], v[222:225], v[188:191], v[148:163]
	ds_read_b128 v[222:225], v2
	s_waitcnt lgkmcnt(0)
; #define SBAR() __builtin_amdgcn_sched_barrier(0)
; #define SLOAD_A(k0) do { const bf16_t* vp_ = Vh + (long)(k0) * LDK + toff; const bf16_t* kp_ = Kh + (long)(k0) * LDK + toff; \
;     sa0 = *(const bf16x8*)kp_; sa1 = *(const bf16x8*)(kp_ + 32L * LDK); sa2 = *(const bf16x8*)vp_; sa3 = *(const bf16x8*)(vp_ + 128); } while (0)
; __device__ __forceinline__ void partialSM(f32x16& p0, f32x16& p1, float& m_reg, float& mn, float& alpha) {
;   constexpr float C = SCALE * 1.4426950408889634f;
;   float pmax = p0[0]; for (int r = 1; r < 16; ++r) pmax = fmaxf(pmax, p0[r]); for (int r = 0; r < 16; ++r) pmax = fmaxf(pmax, p1[r]);
;   { auto rr = __builtin_amdgcn_permlane32_swap(__float_as_uint(pmax), __float_as_uint(pmax), false, false);
;     pmax = fmaxf(__uint_as_float(rr[0]), __uint_as_float(rr[1])); }
;   if (__builtin_expect(__all(pmax - m_reg <= THR / SCALE), 1)) { mn = m_reg; alpha = 1.f; }
;   else { mn = fmaxf(m_reg, pmax); alpha = __builtin_amdgcn_exp2f((m_reg - mn) * C); m_reg = mn; }
;   float mnC = -mn * C;
;   for (int r = 0; r < 16; ++r) p0[r] = fmaf(p0[r], C, mnC); for (int r = 0; r < 16; ++r) p1[r] = fmaf(p1[r], C, mnC);
;   for (int r = 0; r < 16; ++r) p0[r] = __builtin_amdgcn_exp2f(p0[r]);
; }
; __device__ __forceinline__ void finishSM(f32x16& p0, f32x16& p1, float alpha, float& l_reg, bf16x8& pa0, bf16x8& pa1, bf16x8& pa2, bf16x8& pa3) {
;   for (int r = 0; r < 16; ++r) p1[r] = __builtin_amdgcn_exp2f(p1[r]);
;   float ps = 0; for (int r = 0; r < 16; ++r) ps += p0[r]; for (int r = 0; r < 16; ++r) ps += p1[r];
;   { auto rr = __builtin_amdgcn_permlane32_swap(__float_as_uint(ps), __float_as_uint(ps), false, false);
;     ps = __uint_as_float(rr[0]) + __uint_as_float(rr[1]); }
;   l_reg = l_reg * alpha + ps;
;     ...
;   PK4(p0, 0, pa0); PK4(p0, 8, pa1); PK4(p1, 0, pa2); PK4(p1, 8, pa3);
;     ...
; }
; template <int LDQ, int LDK, int LDO>
; __device__ __forceinline__ void attn_body256(const bf16_t* __restrict__ Qb, const bf16_t* __restrict__ Kh, const bf16_t* __restrict__ Vh, float* __restrict__ Ob, int seq, LAS char* lds) {
;     ...
;     if (j + 1 < NT) SLOAD_A((j + 1) * KVBLK);
;     SBAR(); qkt(p0, p1, K_lds + (j & 1) * SHM_K2, qr, r32, hi);
;     partialSM(p0, p1, m_reg, mn, al);
;     finishSM(p0, p1, al, l_reg, pa0, pa1, pa2, pa3); SBAR();
;     if (j + 1 < NT) { asm volatile("s_waitcnt vmcnt(0)" ::: "memory"); SWRITE_A((j + 1) & 1); SLOAD_B((j + 1) * KVBLK); }
	v_mfma_f32_32x32x16_bf16 v[148:163], v[222:225], v[192:195], v[148:163]
	v_mfma_f32_32x32x16_bf16 v[132:147], v[250:253], v[192:195], v[132:147]
	s_nop 9
	v_max_f32_e32 v2, v149, v149
	v_max_f32_e32 v222, v148, v148
	v_max_f32_e32 v2, v222, v2
	v_max3_f32 v2, v2, v150, v151
	v_max3_f32 v2, v2, v152, v153
	v_max3_f32 v2, v2, v154, v155
	v_max3_f32 v2, v2, v156, v157
	v_max3_f32 v2, v2, v158, v159
	v_max3_f32 v2, v2, v160, v161
	v_max3_f32 v2, v2, v162, v163
	v_max3_f32 v2, v2, v132, v133
	v_max3_f32 v2, v2, v134, v135
	v_max3_f32 v2, v2, v136, v137
	v_max3_f32 v2, v2, v138, v139
	v_max3_f32 v2, v2, v140, v141
	v_max3_f32 v2, v2, v142, v143
	v_max3_f32 v2, v2, v144, v145
	v_max3_f32 v2, v2, v146, v147
	v_mov_b32_e32 v222, v2
	s_nop 1
	v_permlane32_swap_b32_e32 v2, v222
	v_max_f32_e32 v222, v222, v222
	v_max_f32_e32 v2, v2, v2
	v_max_f32_e32 v2, v2, v222
	v_sub_f32_e32 v222, v2, v248
	v_cmp_ge_f32_e32 vcc, s8, v222
	s_cmp_eq_u64 vcc, exec
	v_max_f32_e32 v222, v248, v248
	s_cselect_b64 s[10:11], -1, 0
	v_max_f32_e32 v249, v222, v2
	v_cndmask_b32_e64 v2, v249, v248, s[10:11]
	v_mul_f32_e32 v222, 0xbe0293ee, v2
	v_fmamk_f32 v148, v148, 0x3e0293ee, v222
	v_fmamk_f32 v149, v149, 0x3e0293ee, v222
	v_fmamk_f32 v150, v150, 0x3e0293ee, v222
	v_fmamk_f32 v151, v151, 0x3e0293ee, v222
	v_fmamk_f32 v152, v152, 0x3e0293ee, v222
	v_fmamk_f32 v153, v153, 0x3e0293ee, v222
	v_fmamk_f32 v154, v154, 0x3e0293ee, v222
	v_fmamk_f32 v155, v155, 0x3e0293ee, v222
	v_fmamk_f32 v156, v156, 0x3e0293ee, v222
	v_fmamk_f32 v157, v157, 0x3e0293ee, v222
	v_fmamk_f32 v158, v158, 0x3e0293ee, v222
	v_fmamk_f32 v159, v159, 0x3e0293ee, v222
	v_fmamk_f32 v160, v160, 0x3e0293ee, v222
	v_fmamk_f32 v161, v161, 0x3e0293ee, v222
	v_fmamk_f32 v162, v162, 0x3e0293ee, v222
	v_fmamk_f32 v163, v163, 0x3e0293ee, v222
	v_fmamk_f32 v132, v132, 0x3e0293ee, v222
	v_fmamk_f32 v133, v133, 0x3e0293ee, v222
	v_fmamk_f32 v134, v134, 0x3e0293ee, v222
	v_fmamk_f32 v135, v135, 0x3e0293ee, v222
	v_fmamk_f32 v136, v136, 0x3e0293ee, v222
	v_fmamk_f32 v137, v137, 0x3e0293ee, v222
	v_fmamk_f32 v138, v138, 0x3e0293ee, v222
	v_fmamk_f32 v139, v139, 0x3e0293ee, v222
	v_fmamk_f32 v140, v140, 0x3e0293ee, v222
	v_fmamk_f32 v141, v141, 0x3e0293ee, v222
	v_fmamk_f32 v142, v142, 0x3e0293ee, v222
	v_fmamk_f32 v143, v143, 0x3e0293ee, v222
	v_fmamk_f32 v144, v144, 0x3e0293ee, v222
	v_fmamk_f32 v145, v145, 0x3e0293ee, v222
	v_fmamk_f32 v146, v146, 0x3e0293ee, v222
	v_fmac_f32_e32 v222, 0x3e0293ee, v147
	v_exp_f32_e32 v147, v148
	v_exp_f32_e32 v148, v149
	v_exp_f32_e32 v149, v150
	v_exp_f32_e32 v150, v151
	v_exp_f32_e32 v151, v152
	v_exp_f32_e32 v152, v153
	v_exp_f32_e32 v153, v154
	v_exp_f32_e32 v154, v155
	v_exp_f32_e32 v155, v156
	v_exp_f32_e32 v156, v157
	v_exp_f32_e32 v157, v158
	v_exp_f32_e32 v158, v159
	v_exp_f32_e32 v159, v160
	v_exp_f32_e32 v160, v161
	v_exp_f32_e32 v161, v162
	v_exp_f32_e32 v162, v163
	v_exp_f32_e32 v163, v132
	v_add_f32_e32 v132, 0, v147
	v_add_f32_e32 v132, v148, v132
	v_add_f32_e32 v132, v149, v132
	v_add_f32_e32 v132, v150, v132
	v_add_f32_e32 v132, v151, v132
	v_add_f32_e32 v132, v152, v132
	v_add_f32_e32 v132, v153, v132
	v_add_f32_e32 v132, v154, v132
	v_add_f32_e32 v132, v155, v132
	v_add_f32_e32 v132, v156, v132
	v_add_f32_e32 v132, v157, v132
	v_add_f32_e32 v132, v158, v132
	v_add_f32_e32 v132, v159, v132
	v_exp_f32_e32 v223, v133
	v_add_f32_e32 v132, v160, v132
	v_exp_f32_e32 v224, v134
	v_add_f32_e32 v132, v161, v132
	v_exp_f32_e32 v225, v135
	v_add_f32_e32 v132, v162, v132
	v_exp_f32_e32 v250, v136
	v_add_f32_e32 v132, v163, v132
	v_exp_f32_e32 v251, v137
	v_add_f32_e32 v132, v223, v132
	v_exp_f32_e32 v252, v138
	v_add_f32_e32 v132, v224, v132
	v_exp_f32_e32 v253, v139
	v_add_f32_e32 v132, v225, v132
	v_exp_f32_e32 v254, v140
	v_add_f32_e32 v132, v250, v132
	v_exp_f32_e32 v0, v141
	v_add_f32_e32 v132, v251, v132
	v_exp_f32_e32 v1, v142
	v_add_f32_e32 v132, v252, v132
	v_exp_f32_e32 v227, v143
	v_add_f32_e32 v132, v253, v132
	v_exp_f32_e32 v228, v144
	v_add_f32_e32 v132, v254, v132
	v_exp_f32_e32 v229, v145
	v_add_f32_e32 v132, v0, v132
	v_exp_f32_e32 v230, v146
	v_add_f32_e32 v132, v1, v132
	v_exp_f32_e32 v222, v222
	v_add_f32_e32 v132, v227, v132
	v_add_f32_e32 v132, v228, v132
	v_add_f32_e32 v132, v229, v132
	v_add_f32_e32 v132, v230, v132
	v_add_f32_e32 v246, v222, v132
	v_mov_b32_e32 v247, v246
	v_cvt_pk_bf16_f32 v132, v147, v148
	v_cvt_pk_bf16_f32 v133, v149, v150
	v_cvt_pk_bf16_f32 v134, v151, v152
	v_cvt_pk_bf16_f32 v135, v153, v154
	v_cvt_pk_bf16_f32 v136, v155, v156
	v_cvt_pk_bf16_f32 v137, v157, v158
	v_cvt_pk_bf16_f32 v138, v159, v160
	v_cvt_pk_bf16_f32 v139, v161, v162
	v_cvt_pk_bf16_f32 v140, v163, v223
	v_cvt_pk_bf16_f32 v141, v224, v225
	v_cvt_pk_bf16_f32 v142, v250, v251
	v_cvt_pk_bf16_f32 v143, v252, v253
	v_cvt_pk_bf16_f32 v144, v254, v0
	v_cvt_pk_bf16_f32 v145, v1, v227
	v_cvt_pk_bf16_f32 v146, v228, v229
	v_cvt_pk_bf16_f32 v147, v230, v222
	s_nop 1
	v_permlane32_swap_b32_e32 v246, v247
	v_permlane32_swap_b32_e32 v132, v134
	v_permlane32_swap_b32_e32 v133, v135
	v_permlane32_swap_b32_e32 v136, v138
	v_permlane32_swap_b32_e32 v137, v139
	v_permlane32_swap_b32_e32 v140, v142
	v_permlane32_swap_b32_e32 v141, v143
	v_permlane32_swap_b32_e32 v144, v146
	v_permlane32_swap_b32_e32 v145, v147
	s_not_b64 s[8:9], s[84:85]
	s_andn2_b64 vcc, exec, s[84:85]
	s_cbranch_vccnz .LBB0_938
	s_and_b32 s84, s87, 1
	v_lshl_add_u32 v1, s84, 14, v240
	v_add_co_u32_e32 v148, vcc, 0x125000, v220
	s_waitcnt vmcnt(0)
	v_lshl_add_u32 v0, s84, 15, v241
	ds_write_b128 v1, v[204:207]
	ds_write_b128 v1, v[208:211] offset:8192
	v_addc_co_u32_e32 v149, vcc, 0, v221, vcc
	global_load_dwordx4 v[204:207], v[148:149], off
	global_load_dwordx4 v[208:211], v[148:149], off offset:256
	ds_write_b128 v0, v[196:199]
	ds_write_b128 v0, v[200:203] offset:2048
